# flush: accumulator-major W1 MFMAs hidden under sigmoid tails, accumulator zeroing via zero-operand MFMAs inside flush tail, slim re-init
# speedup vs baseline: 1.0474x; 1.0135x over previous
.LBB1_141:
	s_or_b64 exec, exec, s[6:7]
	v_and_b32_e32 v1, 31, v0
	s_waitcnt lgkmcnt(0)
	v_lshlrev_b32_e32 v2, 2, v1
	v_or_b32_e32 v22, 32, v8
	s_barrier
	v_readfirstlane_b32 s95, v9
	s_cmp_lt_u32 s95, 4
	s_cbranch_scc1 .Lstag_done
	s_setprio 1
.Lstag_done:
	v_lshlrev_b32_e32 v3, 2, v22
	global_load_dword v18, v2, s[44:45]
	global_load_dword v19, v2, s[44:45] offset:512
	global_load_dword v20, v2, s[46:47]
	global_load_dword v16, v3, s[44:45]
	global_load_dword v17, v3, s[46:47]
	global_load_dword v12, v2, s[44:45] offset:256
	global_load_dword v13, v2, s[44:45] offset:768
	global_load_dword v15, v2, s[46:47] offset:256
	v_mov_b32_e32 v4, 0x180
	v_lshl_or_b32 v23, v8, 2, v4
	global_load_dword v21, v3, s[44:45] offset:512
	global_load_dword v4, v23, s[44:45]
	global_load_dword v5, v23, s[44:45] offset:512
	global_load_dword v10, v23, s[46:47]
	v_mov_b32_e32 v3, 0x12810
	v_lshl_add_u32 v23, v9, 10, v3
	ds_read2_b32 v[24:25], v23 offset1:32
	v_add_u32_e32 v2, v23, v2
	ds_read2_b32 v[230:231], v2 offset1:1
	v_lshlrev_b32_e32 v26, 8, v9
	s_lshl_b32 s2, s2, 11
	v_or3_b32 v235, v26, s2, v1
	s_mov_b32 s12, 0x7a120
	s_waitcnt lgkmcnt(1)
	v_readfirstlane_b32 s13, v24
	v_readfirstlane_b32 s6, v25
	v_cmp_gt_i32_e32 vcc, s12, v235
	v_mov_b32_e32 v2, 0
	v_mov_b32_e32 v238, 0
	s_and_saveexec_b64 s[2:3], vcc
	s_cbranch_execz .LBB1_143
	v_ashrrev_i32_e32 v25, 31, v235
	v_mov_b32_e32 v24, v235
	v_lshl_add_u64 v[24:25], v[24:25], 2, s[50:51]
	global_load_dword v238, v[24:25], off

.LBB1_146:
	s_or_b64 exec, exec, s[10:11]
	v_mov_b64_e32 v[234:235], v[16:17]
	s_mov_b64 s[10:11], exec
	v_mov_b32_e32 v251, v82
	v_mov_b32_e32 v231, v249
	v_mov_b32_e32 v249, s20

.LBB1_153:
	s_or_b64 exec, exec, s[2:3]
	v_cmp_ge_i32_e32 vcc, s18, v249
	s_mov_b64 s[8:9], 0
	s_and_saveexec_b64 s[2:3], vcc
	s_cbranch_execz .LBB1_148
	v_cmp_gt_i32_e32 vcc, s12, v235
	s_and_b64 s[10:11], s[0:1], vcc
	ds_read_b128 v[82:85], v245 offset:32768
	ds_read_b128 v[86:89], v245 offset:32784
	ds_read_b128 v[90:93], v245 offset:32800
	ds_read_b128 v[94:97], v245 offset:32816
	ds_read_b128 v[98:101], v245 offset:32832
	ds_read_b128 v[102:105], v245 offset:32848
	ds_read_b128 v[106:109], v245 offset:32864
	ds_read_b128 v[110:113], v245 offset:32880
	ds_read_b128 v[114:117], v246 offset:0
	ds_read_b128 v[118:121], v246 offset:8192
	ds_read_b128 v[122:125], v246 offset:1024
	ds_read_b128 v[126:129], v246 offset:9216
	v_cvt_f32_i32_e32 v16, v234
	v_cvt_pk_f16_f32 v4, v66, v67
	v_cvt_pk_f16_f32 v5, v68, v69
	v_cvt_pk_f16_f32 v6, v70, v71
	v_cvt_pk_f16_f32 v7, v72, v73
	v_cvt_pk_f16_f32 v8, v74, v75
	v_cvt_pk_f16_f32 v9, v76, v77
	v_cvt_pk_f16_f32 v10, v78, v79
	v_cvt_pk_f16_f32 v11, v80, v81
	s_waitcnt lgkmcnt(8)
	v_pk_mul_f32 v[162:163], v[82:83], v[16:17] op_sel_hi:[1,0]
	v_pk_mul_f32 v[164:165], v[84:85], v[16:17] op_sel_hi:[1,0]
	v_pk_mul_f32 v[166:167], v[86:87], v[16:17] op_sel_hi:[1,0]
	v_pk_mul_f32 v[168:169], v[88:89], v[16:17] op_sel_hi:[1,0]
	v_pk_mul_f32 v[170:171], v[90:91], v[16:17] op_sel_hi:[1,0]
	v_pk_mul_f32 v[172:173], v[92:93], v[16:17] op_sel_hi:[1,0]
	v_pk_mul_f32 v[174:175], v[94:95], v[16:17] op_sel_hi:[1,0]
	v_pk_mul_f32 v[176:177], v[96:97], v[16:17] op_sel_hi:[1,0]
	ds_read_b128 v[130:133], v246 offset:2048
	ds_read_b128 v[134:137], v246 offset:10240
	ds_read_b128 v[138:141], v246 offset:3072
	ds_read_b128 v[142:145], v246 offset:11264
	s_waitcnt lgkmcnt(4)
	v_mfma_f32_32x32x16_f16 v[162:177], v[114:117], v[4:7], v[162:177]
	v_pk_mul_f32 v[146:147], v[98:99], v[16:17] op_sel_hi:[1,0]
	v_pk_mul_f32 v[148:149], v[100:101], v[16:17] op_sel_hi:[1,0]
	v_pk_mul_f32 v[150:151], v[102:103], v[16:17] op_sel_hi:[1,0]
	v_pk_mul_f32 v[152:153], v[104:105], v[16:17] op_sel_hi:[1,0]
	v_pk_mul_f32 v[154:155], v[106:107], v[16:17] op_sel_hi:[1,0]
	v_pk_mul_f32 v[156:157], v[108:109], v[16:17] op_sel_hi:[1,0]
	v_pk_mul_f32 v[158:159], v[110:111], v[16:17] op_sel_hi:[1,0]
	v_pk_mul_f32 v[160:161], v[112:113], v[16:17] op_sel_hi:[1,0]
	s_nop 1
	v_mfma_f32_32x32x16_f16 v[146:161], v[118:121], v[4:7], v[146:161]
	v_cvt_pk_f16_f32 v12, v50, v51
	v_cvt_pk_f16_f32 v13, v52, v53
	v_cvt_pk_f16_f32 v14, v54, v55
	v_cvt_pk_f16_f32 v15, v56, v57
	v_mfma_f32_32x32x16_f16 v[162:177], v[122:125], v[8:11], v[162:177]
	v_cvt_pk_f16_f32 v252, v58, v59
	v_cvt_pk_f16_f32 v253, v60, v61
	v_cvt_pk_f16_f32 v254, v62, v63
	v_cvt_pk_f16_f32 v255, v64, v65
	v_mfma_f32_32x32x16_f16 v[146:161], v[126:129], v[8:11], v[146:161]
	ds_read_b128 v[82:85], v246 offset:4096
	ds_read_b128 v[86:89], v246 offset:12288
	ds_read_b128 v[90:93], v246 offset:5120
	ds_read_b128 v[94:97], v246 offset:13312
	s_waitcnt lgkmcnt(4)
	v_mfma_f32_32x32x16_f16 v[162:177], v[130:133], v[12:15], v[162:177]
	v_cvt_pk_f16_f32 v4, v34, v35
	v_cvt_pk_f16_f32 v5, v36, v37
	v_mfma_f32_32x32x16_f16 v[146:161], v[134:137], v[12:15], v[146:161]
	v_cvt_pk_f16_f32 v6, v38, v39
	v_cvt_pk_f16_f32 v7, v40, v41
	v_mfma_f32_32x32x16_f16 v[162:177], v[138:141], v[252:255], v[162:177]
	v_cvt_pk_f16_f32 v8, v42, v43
	v_cvt_pk_f16_f32 v9, v44, v45
	v_mfma_f32_32x32x16_f16 v[146:161], v[142:145], v[252:255], v[146:161]
	v_cvt_pk_f16_f32 v10, v46, v47
	v_cvt_pk_f16_f32 v11, v48, v49
	ds_read_b128 v[98:101], v246 offset:6144
	ds_read_b128 v[102:105], v246 offset:14336
	ds_read_b128 v[106:109], v246 offset:7168
	ds_read_b128 v[110:113], v246 offset:15360
	s_waitcnt lgkmcnt(4)
	v_mfma_f32_32x32x16_f16 v[162:177], v[82:85], v[4:7], v[162:177]
	v_cvt_pk_f16_f32 v12, v18, v19
	v_cvt_pk_f16_f32 v13, v20, v21
	v_mfma_f32_32x32x16_f16 v[146:161], v[86:89], v[4:7], v[146:161]
	v_cvt_pk_f16_f32 v14, v22, v23
	v_cvt_pk_f16_f32 v15, v24, v25
	v_mfma_f32_32x32x16_f16 v[162:177], v[90:93], v[8:11], v[162:177]
	v_cvt_pk_f16_f32 v252, v26, v27
	v_cvt_pk_f16_f32 v253, v28, v29
	v_mfma_f32_32x32x16_f16 v[146:161], v[94:97], v[8:11], v[146:161]
	v_cvt_pk_f16_f32 v254, v30, v31
	v_cvt_pk_f16_f32 v255, v32, v33
	ds_read_b128 v[18:21], v246 offset:16384
	ds_read_b128 v[22:25], v246 offset:17408
	ds_read_b128 v[26:29], v246 offset:18432
	ds_read_b128 v[30:33], v246 offset:19456
	s_waitcnt lgkmcnt(4)
	v_mfma_f32_32x32x16_f16 v[162:177], v[98:101], v[12:15], v[162:177]
	v_mfma_f32_32x32x16_f16 v[146:161], v[102:105], v[12:15], v[146:161]
	v_mfma_f32_32x32x16_f16 v[162:177], v[106:109], v[252:255], v[162:177]
	v_mfma_f32_32x32x16_f16 v[146:161], v[110:113], v[252:255], v[146:161]
	ds_read_b128 v[130:133], v247 offset:33024
	ds_read_b128 v[134:137], v247 offset:33040
	ds_read_b128 v[138:141], v247 offset:33056
	ds_read_b128 v[142:145], v247 offset:33072
	ds_read_b128 v[114:117], v247 offset:33088
	ds_read_b128 v[118:121], v247 offset:33104
	ds_read_b128 v[122:125], v247 offset:33120
	ds_read_b128 v[126:129], v247 offset:33136
	s_nop 2
	v_cvt_pk_f16_f32 v4, v162, v163
	v_cvt_pk_f16_f32 v5, v164, v165
	v_cvt_pk_f16_f32 v6, v166, v167
	v_cvt_pk_f16_f32 v7, v168, v169
	v_cvt_pk_f16_f32 v8, v170, v171
	v_cvt_pk_f16_f32 v9, v172, v173
	v_cvt_pk_f16_f32 v10, v174, v175
	v_cvt_pk_f16_f32 v11, v176, v177
	v_cvt_pk_f16_f32 v12, v146, v147
	v_cvt_pk_f16_f32 v13, v148, v149
	v_cvt_pk_f16_f32 v14, v150, v151
	v_cvt_pk_f16_f32 v15, v152, v153
	v_cvt_pk_f16_f32 v252, v154, v155
	v_cvt_pk_f16_f32 v253, v156, v157
	v_cvt_pk_f16_f32 v254, v158, v159
	v_cvt_pk_f16_f32 v255, v160, v161
	s_waitcnt lgkmcnt(4)
	ds_read_b128 v[34:37], v246 offset:20480
	ds_read_b128 v[38:41], v246 offset:21504
	ds_read_b128 v[42:45], v246 offset:22528
	ds_read_b128 v[46:49], v246 offset:23552
	v_mfma_f32_32x32x16_f16 v[130:145], v[18:21], v[4:7], v[130:145]
	v_mfma_f32_32x32x16_f16 v[130:145], v[22:25], v[8:11], v[130:145]
	v_mfma_f32_32x32x16_f16 v[130:145], v[26:29], v[12:15], v[130:145]
	v_mfma_f32_32x32x16_f16 v[130:145], v[30:33], v[252:255], v[130:145]
	ds_read_b128 v[146:149], v247 offset:33536
	ds_read_b128 v[150:153], v247 offset:33552
	ds_read_b128 v[154:157], v247 offset:33568
	ds_read_b128 v[158:161], v247 offset:33584
	s_waitcnt lgkmcnt(4)
	ds_read_b128 v[98:101], v247 offset:33152
	ds_read_b128 v[102:105], v247 offset:33168
	ds_read_b128 v[106:109], v247 offset:33184
	ds_read_b128 v[110:113], v247 offset:33200
	ds_read_b128 v[50:53], v246 offset:24576
	ds_read_b128 v[54:57], v246 offset:25600
	ds_read_b128 v[58:61], v246 offset:26624
	ds_read_b128 v[62:65], v246 offset:27648
	v_mfma_f32_32x32x16_f16 v[114:129], v[34:37], v[4:7], v[114:129]
	v_exp_f32_e32 v130, v130
	v_exp_f32_e32 v131, v131
	v_exp_f32_e32 v132, v132
	v_exp_f32_e32 v133, v133
	v_exp_f32_e32 v134, v134
	v_exp_f32_e32 v135, v135
	v_exp_f32_e32 v136, v136
	v_exp_f32_e32 v137, v137
	v_mfma_f32_32x32x16_f16 v[114:129], v[38:41], v[8:11], v[114:129]
	v_exp_f32_e32 v138, v138
	v_exp_f32_e32 v139, v139
	v_exp_f32_e32 v140, v140
	v_exp_f32_e32 v141, v141
	v_exp_f32_e32 v142, v142
	v_exp_f32_e32 v143, v143
	v_exp_f32_e32 v144, v144
	v_exp_f32_e32 v145, v145
	v_mfma_f32_32x32x16_f16 v[114:129], v[42:45], v[12:15], v[114:129]
	v_add_f32_e32 v130, 1.0, v130
	v_add_f32_e32 v131, 1.0, v131
	v_add_f32_e32 v132, 1.0, v132
	v_add_f32_e32 v133, 1.0, v133
	v_add_f32_e32 v134, 1.0, v134
	v_add_f32_e32 v135, 1.0, v135
	v_add_f32_e32 v136, 1.0, v136
	v_add_f32_e32 v137, 1.0, v137
	v_add_f32_e32 v138, 1.0, v138
	v_add_f32_e32 v139, 1.0, v139
	v_add_f32_e32 v140, 1.0, v140
	v_add_f32_e32 v141, 1.0, v141
	v_add_f32_e32 v142, 1.0, v142
	v_add_f32_e32 v143, 1.0, v143
	v_add_f32_e32 v144, 1.0, v144
	v_add_f32_e32 v145, 1.0, v145
	v_mfma_f32_32x32x16_f16 v[114:129], v[46:49], v[252:255], v[114:129]
	v_rcp_f32_e32 v130, v130
	v_rcp_f32_e32 v131, v131
	v_rcp_f32_e32 v132, v132
	v_rcp_f32_e32 v133, v133
	v_rcp_f32_e32 v134, v134
	v_rcp_f32_e32 v135, v135
	v_rcp_f32_e32 v136, v136
	v_rcp_f32_e32 v137, v137
	v_rcp_f32_e32 v138, v138
	v_rcp_f32_e32 v139, v139
	v_rcp_f32_e32 v140, v140
	v_rcp_f32_e32 v141, v141
	v_rcp_f32_e32 v142, v142
	v_rcp_f32_e32 v143, v143
	v_rcp_f32_e32 v144, v144
	v_rcp_f32_e32 v145, v145
	s_waitcnt lgkmcnt(8)
	ds_read_b128 v[162:165], v247 offset:33600
	ds_read_b128 v[166:169], v247 offset:33616
	ds_read_b128 v[170:173], v247 offset:33632
	ds_read_b128 v[174:177], v247 offset:33648
	v_mul_f32_e32 v3, v146, v130
	v_mul_f32_e32 v16, v147, v131
	v_mul_f32_e32 v17, v148, v132
	v_fmac_f32_e32 v3, v149, v133
	v_fmac_f32_e32 v16, v150, v134
	v_fmac_f32_e32 v17, v151, v135
	v_fmac_f32_e32 v3, v152, v136
	v_fmac_f32_e32 v16, v153, v137
	v_fmac_f32_e32 v17, v154, v138
	v_fmac_f32_e32 v3, v155, v139
	v_fmac_f32_e32 v16, v156, v140
	v_fmac_f32_e32 v17, v157, v141
	v_fmac_f32_e32 v3, v158, v142
	v_fmac_f32_e32 v16, v159, v143
	v_fmac_f32_e32 v17, v160, v144
	v_fmac_f32_e32 v3, v161, v145
	s_waitcnt lgkmcnt(4)
	ds_read_b128 v[82:85], v247 offset:33216
	ds_read_b128 v[86:89], v247 offset:33232
	ds_read_b128 v[90:93], v247 offset:33248
	ds_read_b128 v[94:97], v247 offset:33264
	ds_read_b128 v[66:69], v246 offset:28672
	ds_read_b128 v[70:73], v246 offset:29696
	ds_read_b128 v[74:77], v246 offset:30720
	ds_read_b128 v[78:81], v246 offset:31744
	v_mfma_f32_32x32x16_f16 v[98:113], v[50:53], v[4:7], v[98:113]
	v_exp_f32_e32 v114, v114
	v_exp_f32_e32 v115, v115
	v_exp_f32_e32 v116, v116
	v_exp_f32_e32 v117, v117
	v_exp_f32_e32 v118, v118
	v_exp_f32_e32 v119, v119
	v_exp_f32_e32 v120, v120
	v_exp_f32_e32 v121, v121
	v_mfma_f32_32x32x16_f16 v[98:113], v[54:57], v[8:11], v[98:113]
	v_exp_f32_e32 v122, v122
	v_exp_f32_e32 v123, v123
	v_exp_f32_e32 v124, v124
	v_exp_f32_e32 v125, v125
	v_exp_f32_e32 v126, v126
	v_exp_f32_e32 v127, v127
	v_exp_f32_e32 v128, v128
	v_exp_f32_e32 v129, v129
	v_mfma_f32_32x32x16_f16 v[98:113], v[58:61], v[12:15], v[98:113]
	v_add_f32_e32 v114, 1.0, v114
	v_add_f32_e32 v115, 1.0, v115
	v_add_f32_e32 v116, 1.0, v116
	v_add_f32_e32 v117, 1.0, v117
	v_add_f32_e32 v118, 1.0, v118
	v_add_f32_e32 v119, 1.0, v119
	v_add_f32_e32 v120, 1.0, v120
	v_add_f32_e32 v121, 1.0, v121
	v_add_f32_e32 v122, 1.0, v122
	v_add_f32_e32 v123, 1.0, v123
	v_add_f32_e32 v124, 1.0, v124
	v_add_f32_e32 v125, 1.0, v125
	v_add_f32_e32 v126, 1.0, v126
	v_add_f32_e32 v127, 1.0, v127
	v_add_f32_e32 v128, 1.0, v128
	v_add_f32_e32 v129, 1.0, v129
	v_mfma_f32_32x32x16_f16 v[98:113], v[62:65], v[252:255], v[98:113]
	v_rcp_f32_e32 v114, v114
	v_rcp_f32_e32 v115, v115
	v_rcp_f32_e32 v116, v116
	v_rcp_f32_e32 v117, v117
	v_rcp_f32_e32 v118, v118
	v_rcp_f32_e32 v119, v119
	v_rcp_f32_e32 v120, v120
	v_rcp_f32_e32 v121, v121
	v_rcp_f32_e32 v122, v122
	v_rcp_f32_e32 v123, v123
	v_rcp_f32_e32 v124, v124
	v_rcp_f32_e32 v125, v125
	v_rcp_f32_e32 v126, v126
	v_rcp_f32_e32 v127, v127
	v_rcp_f32_e32 v128, v128
	v_rcp_f32_e32 v129, v129
	s_waitcnt lgkmcnt(8)
	ds_read_b128 v[18:21], v247 offset:33664
	ds_read_b128 v[22:25], v247 offset:33680
	ds_read_b128 v[26:29], v247 offset:33696
	ds_read_b128 v[30:33], v247 offset:33712
	v_fmac_f32_e32 v3, v162, v114
	v_fmac_f32_e32 v16, v163, v115
	v_fmac_f32_e32 v17, v164, v116
	v_fmac_f32_e32 v3, v165, v117
	v_fmac_f32_e32 v16, v166, v118
	v_fmac_f32_e32 v17, v167, v119
	v_fmac_f32_e32 v3, v168, v120
	v_fmac_f32_e32 v16, v169, v121
	v_fmac_f32_e32 v17, v170, v122
	v_fmac_f32_e32 v3, v171, v123
	v_fmac_f32_e32 v16, v172, v124
	v_fmac_f32_e32 v17, v173, v125
	v_fmac_f32_e32 v3, v174, v126
	v_fmac_f32_e32 v16, v175, v127
	v_fmac_f32_e32 v17, v176, v128
	v_fmac_f32_e32 v3, v177, v129
	s_waitcnt lgkmcnt(4)
	ds_read_b128 v[146:149], v247 offset:33728
	ds_read_b128 v[150:153], v247 offset:33744
	ds_read_b128 v[154:157], v247 offset:33760
	ds_read_b128 v[158:161], v247 offset:33776
	v_mfma_f32_32x32x16_f16 v[82:97], v[66:69], v[4:7], v[82:97]
	v_exp_f32_e32 v98, v98
	v_exp_f32_e32 v99, v99
	v_exp_f32_e32 v100, v100
	v_exp_f32_e32 v101, v101
	v_exp_f32_e32 v102, v102
	v_exp_f32_e32 v103, v103
	v_exp_f32_e32 v104, v104
	v_exp_f32_e32 v105, v105
	v_mfma_f32_32x32x16_f16 v[82:97], v[70:73], v[8:11], v[82:97]
	v_exp_f32_e32 v106, v106
	v_exp_f32_e32 v107, v107
	v_exp_f32_e32 v108, v108
	v_exp_f32_e32 v109, v109
	v_exp_f32_e32 v110, v110
	v_exp_f32_e32 v111, v111
	v_exp_f32_e32 v112, v112
	v_exp_f32_e32 v113, v113
	v_mfma_f32_32x32x16_f16 v[82:97], v[74:77], v[12:15], v[82:97]
	v_add_f32_e32 v98, 1.0, v98
	v_add_f32_e32 v99, 1.0, v99
	v_add_f32_e32 v100, 1.0, v100
	v_add_f32_e32 v101, 1.0, v101
	v_add_f32_e32 v102, 1.0, v102
	v_add_f32_e32 v103, 1.0, v103
	v_add_f32_e32 v104, 1.0, v104
	v_add_f32_e32 v105, 1.0, v105
	v_add_f32_e32 v106, 1.0, v106
	v_add_f32_e32 v107, 1.0, v107
	v_add_f32_e32 v108, 1.0, v108
	v_add_f32_e32 v109, 1.0, v109
	v_add_f32_e32 v110, 1.0, v110
	v_add_f32_e32 v111, 1.0, v111
	v_add_f32_e32 v112, 1.0, v112
	v_add_f32_e32 v113, 1.0, v113
	v_mfma_f32_32x32x16_f16 v[82:97], v[78:81], v[252:255], v[82:97]
	v_rcp_f32_e32 v98, v98
	v_rcp_f32_e32 v99, v99
	v_rcp_f32_e32 v100, v100
	v_rcp_f32_e32 v101, v101
	v_rcp_f32_e32 v102, v102
	v_rcp_f32_e32 v103, v103
	v_rcp_f32_e32 v104, v104
	v_rcp_f32_e32 v105, v105
	v_rcp_f32_e32 v106, v106
	v_rcp_f32_e32 v107, v107
	v_rcp_f32_e32 v108, v108
	v_rcp_f32_e32 v109, v109
	v_rcp_f32_e32 v110, v110
	v_rcp_f32_e32 v111, v111
	v_rcp_f32_e32 v112, v112
	v_rcp_f32_e32 v113, v113
	s_waitcnt lgkmcnt(4)
	v_fmac_f32_e32 v3, v18, v98
	v_fmac_f32_e32 v16, v19, v99
	v_fmac_f32_e32 v17, v20, v100
	v_fmac_f32_e32 v3, v21, v101
	v_fmac_f32_e32 v16, v22, v102
	v_fmac_f32_e32 v17, v23, v103
	v_fmac_f32_e32 v3, v24, v104
	v_fmac_f32_e32 v16, v25, v105
	v_fmac_f32_e32 v17, v26, v106
	v_fmac_f32_e32 v3, v27, v107
	v_fmac_f32_e32 v16, v28, v108
	v_fmac_f32_e32 v17, v29, v109
	v_fmac_f32_e32 v3, v30, v110
	v_fmac_f32_e32 v16, v31, v111
	v_fmac_f32_e32 v17, v32, v112
	v_fmac_f32_e32 v3, v33, v113
	v_mov_b32_e32 v4, 0
	v_mov_b32_e32 v5, 0
	v_mov_b32_e32 v6, 0
	v_mov_b32_e32 v7, 0
	v_exp_f32_e32 v82, v82
	v_exp_f32_e32 v83, v83
	v_exp_f32_e32 v84, v84
	v_exp_f32_e32 v85, v85
	v_exp_f32_e32 v86, v86
	v_exp_f32_e32 v87, v87
	v_exp_f32_e32 v88, v88
	v_exp_f32_e32 v89, v89
	v_mfma_f32_32x32x16_f16 v[66:81], v[4:7], v[4:7], 0
	v_exp_f32_e32 v90, v90
	v_exp_f32_e32 v91, v91
	v_exp_f32_e32 v92, v92
	v_exp_f32_e32 v93, v93
	v_exp_f32_e32 v94, v94
	v_exp_f32_e32 v95, v95
	v_exp_f32_e32 v96, v96
	v_exp_f32_e32 v97, v97
	v_mfma_f32_32x32x16_f16 v[50:65], v[4:7], v[4:7], 0
	v_add_f32_e32 v82, 1.0, v82
	v_add_f32_e32 v83, 1.0, v83
	v_add_f32_e32 v84, 1.0, v84
	v_add_f32_e32 v85, 1.0, v85
	v_add_f32_e32 v86, 1.0, v86
	v_add_f32_e32 v87, 1.0, v87
	v_add_f32_e32 v88, 1.0, v88
	v_add_f32_e32 v89, 1.0, v89
	v_add_f32_e32 v90, 1.0, v90
	v_add_f32_e32 v91, 1.0, v91
	v_add_f32_e32 v92, 1.0, v92
	v_add_f32_e32 v93, 1.0, v93
	v_add_f32_e32 v94, 1.0, v94
	v_add_f32_e32 v95, 1.0, v95
	v_add_f32_e32 v96, 1.0, v96
	v_add_f32_e32 v97, 1.0, v97
	v_mfma_f32_32x32x16_f16 v[34:49], v[4:7], v[4:7], 0
	v_rcp_f32_e32 v82, v82
	v_rcp_f32_e32 v83, v83
	v_rcp_f32_e32 v84, v84
	v_rcp_f32_e32 v85, v85
	v_rcp_f32_e32 v86, v86
	v_rcp_f32_e32 v87, v87
	v_rcp_f32_e32 v88, v88
	v_rcp_f32_e32 v89, v89
	v_rcp_f32_e32 v90, v90
	v_rcp_f32_e32 v91, v91
	v_rcp_f32_e32 v92, v92
	v_rcp_f32_e32 v93, v93
	v_rcp_f32_e32 v94, v94
	v_rcp_f32_e32 v95, v95
	v_rcp_f32_e32 v96, v96
	v_rcp_f32_e32 v97, v97
	s_waitcnt lgkmcnt(0)
	v_mfma_f32_32x32x16_f16 v[18:33], v[4:7], v[4:7], 0
	v_fmac_f32_e32 v3, v146, v82
	v_fmac_f32_e32 v16, v147, v83
	v_fmac_f32_e32 v17, v148, v84
	v_fmac_f32_e32 v3, v149, v85
	v_fmac_f32_e32 v16, v150, v86
	v_fmac_f32_e32 v17, v151, v87
	v_fmac_f32_e32 v3, v152, v88
	v_fmac_f32_e32 v16, v153, v89
	v_fmac_f32_e32 v17, v154, v90
	v_fmac_f32_e32 v3, v155, v91
	v_fmac_f32_e32 v16, v156, v92
	v_fmac_f32_e32 v17, v157, v93
	v_fmac_f32_e32 v3, v158, v94
	v_fmac_f32_e32 v16, v159, v95
	v_fmac_f32_e32 v17, v160, v96
	v_fmac_f32_e32 v3, v161, v97
	v_add_f32_e32 v3, v3, v16
	v_add_f32_e32 v3, v3, v17
	ds_bpermute_b32 v4, v248, v3
	s_and_saveexec_b64 s[8:9], s[10:11]
	s_cbranch_execz .LBB1_156
	s_waitcnt vmcnt(0)
	v_mul_f32_e32 v5, 0x40549a78, v238
	v_exp_f32_e32 v5, v5
	s_waitcnt lgkmcnt(0)
	v_add_f32_e32 v3, v3, v4
	v_ashrrev_i32_e32 v7, 31, v235
	v_mov_b32_e32 v6, v235
	v_add_f32_e32 v3, v239, v3
	v_lshl_add_u64 v[6:7], v[6:7], 2, s[52:53]
	v_mul_f32_e32 v3, v5, v3
	global_store_dword v[6:7], v3, off
.LBB1_156:
	s_or_b64 exec, exec, s[8:9]
	v_add_u32_e32 v82, 1, v251
	v_cmp_ne_u32_e32 vcc, v82, v242
	s_mov_b64 s[10:11], 0
	v_mov_b32_e32 v251, v242
	s_and_saveexec_b64 s[8:9], vcc
	s_cbranch_execz .LBB1_147
	v_lshlrev_b32_e32 v3, 7, v82
	s_waitcnt lgkmcnt(0)
	v_add_u32_e32 v4, v244, v3
	v_add_u32_e32 v3, 0x12890, v3
	ds_read_b32 v3, v3
	ds_read2_b32 v[230:231], v4 offset1:1
	v_add_u32_e32 v17, 32, v235
	v_cmp_gt_i32_e32 vcc, s17, v235
	v_mov_b32_e32 v238, 0
	s_waitcnt lgkmcnt(0)
	v_readfirstlane_b32 s20, v3
	v_sub_u32_e32 v16, v231, v230
	s_and_saveexec_b64 s[10:11], vcc
	s_cbranch_execz .LBB1_146
	v_ashrrev_i32_e32 v5, 31, v17
	v_mov_b32_e32 v4, v17
	v_lshl_add_u64 v[4:5], v[4:5], 2, s[50:51]
	global_load_dword v238, v[4:5], off
	s_branch .LBB1_146
